# layer-1 table conversion in P1: non-temporal hint on the read-once f32 row loads (touches stay plain)
# speedup vs baseline: 1.0047x; 1.0047x over previous
.LBB0_447:
	s_andn2_b64 vcc, exec, s[6:7]
	s_cbranch_vccnz .LBB0_450
	s_cmp_lg_u32 s3, 0
	s_cbranch_scc1 .LBB0_450
	s_lshl_b32 s5, s20, 6
	s_add_i32 s5, s5, s4
	v_or_b32_e32 v86, s5, v1
	s_ashr_i32 s5, s5, 31
	s_lshr_b32 s5, s5, 19
	v_add_u32_e32 v2, s5, v86
	v_and_b32_e32 v2, 0xfffe000, v2
	v_sub_u32_e32 v2, v86, v2
	v_lshlrev_b32_e32 v70, 4, v2
	v_ashrrev_i32_e32 v71, 31, v70
	v_lshlrev_b64 v[78:79], 2, v[70:71]
	v_lshlrev_b32_e32 v2, 5, v68
	v_lshl_add_u64 v[70:71], s[74:75], 0, v[78:79]
	v_lshl_add_u64 v[74:75], v[70:71], 0, v[2:3]
	v_lshl_add_u64 v[78:79], s[72:73], 0, v[78:79]
	global_load_dwordx4 v[70:73], v[74:75], off nt
	s_nop 0
	global_load_dwordx4 v[74:77], v[74:75], off offset:16 nt
	v_lshl_add_u64 v[82:83], v[78:79], 0, v[2:3]
	global_load_dwordx4 v[78:81], v[82:83], off nt
	s_nop 0
	global_load_dwordx4 v[82:85], v[82:83], off offset:16 nt
	v_or_b32_e32 v90, 32, v86
	v_add_u32_e32 v69, s5, v90
	v_and_b32_e32 v69, 0xfffe000, v69
	v_sub_u32_e32 v69, v90, v69
	v_ashrrev_i32_e32 v87, 31, v86
	v_lshlrev_b32_e32 v92, 4, v69
	v_lshlrev_b64 v[86:87], 6, v[86:87]
	v_ashrrev_i32_e32 v93, 31, v92
	v_lshlrev_b32_e32 v88, 4, v68
	v_mov_b32_e32 v89, v3
	v_lshl_add_u64 v[86:87], s[52:53], 0, v[86:87]
	v_lshlrev_b64 v[92:93], 2, v[92:93]
	v_lshl_add_u64 v[86:87], v[86:87], 0, v[88:89]
	v_lshl_add_u64 v[94:95], s[74:75], 0, v[92:93]
	v_lshl_add_u64 v[94:95], v[94:95], 0, v[2:3]
	v_ashrrev_i32_e32 v91, 31, v90
	s_waitcnt vmcnt(3)
	v_pk_mul_f32 v[96:97], v[60:61], v[70:71]
	v_pk_mul_f32 v[98:99], v[62:63], v[72:73]
	v_pk_mul_f32 v[72:73], v[54:55], v[72:73]
	s_waitcnt vmcnt(2)
	v_pk_mul_f32 v[100:101], v[64:65], v[74:75]
	v_pk_mul_f32 v[74:75], v[56:57], v[74:75]
	v_pk_mul_f32 v[102:103], v[66:67], v[76:77]
	v_pk_mul_f32 v[70:71], v[52:53], v[70:71]
	v_pk_mul_f32 v[76:77], v[58:59], v[76:77]
	s_waitcnt vmcnt(1)
	v_pk_fma_f32 v[96:97], v[52:53], v[78:79], v[96:97] neg_lo:[0,0,1] neg_hi:[0,0,1]
	v_pk_fma_f32 v[98:99], v[54:55], v[80:81], v[98:99] neg_lo:[0,0,1] neg_hi:[0,0,1]
	v_pk_fma_f32 v[80:81], v[62:63], v[80:81], v[72:73]
	s_waitcnt vmcnt(0)
	v_pk_fma_f32 v[72:73], v[56:57], v[82:83], v[100:101] neg_lo:[0,0,1] neg_hi:[0,0,1]
	v_pk_fma_f32 v[82:83], v[64:65], v[82:83], v[74:75]
	v_pk_fma_f32 v[74:75], v[58:59], v[84:85], v[102:103] neg_lo:[0,0,1] neg_hi:[0,0,1]
	v_pk_fma_f32 v[78:79], v[60:61], v[78:79], v[70:71]
	v_pk_fma_f32 v[84:85], v[66:67], v[84:85], v[76:77]
	v_cvt_pk_bf16_f32 v70, v96, v97
	v_cvt_pk_bf16_f32 v71, v98, v99
	v_cvt_pk_bf16_f32 v72, v72, v73
	v_cvt_pk_bf16_f32 v73, v74, v75
	v_cvt_pk_bf16_f32 v74, v78, v79
	v_cvt_pk_bf16_f32 v75, v80, v81
	v_cvt_pk_bf16_f32 v76, v82, v83
	v_cvt_pk_bf16_f32 v77, v84, v85
	global_store_dwordx4 v[86:87], v[70:73], off
	global_store_dwordx4 v[86:87], v[74:77], off offset:32
	v_lshl_add_u64 v[78:79], s[72:73], 0, v[92:93]
	global_load_dwordx4 v[70:73], v[94:95], off nt
	global_load_dwordx4 v[74:77], v[94:95], off offset:16 nt
	v_lshl_add_u64 v[82:83], v[78:79], 0, v[2:3]
	global_load_dwordx4 v[78:81], v[82:83], off nt
	s_nop 0
	global_load_dwordx4 v[82:85], v[82:83], off offset:16 nt
	v_lshlrev_b64 v[86:87], 6, v[90:91]
	v_lshl_add_u64 v[86:87], s[52:53], 0, v[86:87]
	v_lshl_add_u64 v[86:87], v[86:87], 0, v[88:89]
	s_waitcnt vmcnt(3)
	v_pk_mul_f32 v[88:89], v[44:45], v[70:71]
	v_pk_mul_f32 v[90:91], v[46:47], v[72:73]
	v_pk_mul_f32 v[72:73], v[38:39], v[72:73]
	s_waitcnt vmcnt(2)
	v_pk_mul_f32 v[92:93], v[48:49], v[74:75]
	v_pk_mul_f32 v[74:75], v[40:41], v[74:75]
	v_pk_mul_f32 v[94:95], v[50:51], v[76:77]
	v_pk_mul_f32 v[70:71], v[36:37], v[70:71]
	v_pk_mul_f32 v[76:77], v[42:43], v[76:77]
	s_waitcnt vmcnt(1)
	v_pk_fma_f32 v[88:89], v[36:37], v[78:79], v[88:89] neg_lo:[0,0,1] neg_hi:[0,0,1]
	v_pk_fma_f32 v[90:91], v[38:39], v[80:81], v[90:91] neg_lo:[0,0,1] neg_hi:[0,0,1]
	v_pk_fma_f32 v[80:81], v[46:47], v[80:81], v[72:73]
	s_waitcnt vmcnt(0)
	v_pk_fma_f32 v[72:73], v[40:41], v[82:83], v[92:93] neg_lo:[0,0,1] neg_hi:[0,0,1]
	v_pk_fma_f32 v[82:83], v[48:49], v[82:83], v[74:75]
	v_pk_fma_f32 v[74:75], v[42:43], v[84:85], v[94:95] neg_lo:[0,0,1] neg_hi:[0,0,1]
	v_pk_fma_f32 v[78:79], v[44:45], v[78:79], v[70:71]
	v_pk_fma_f32 v[84:85], v[50:51], v[84:85], v[76:77]
	v_cvt_pk_bf16_f32 v70, v88, v89
	v_cvt_pk_bf16_f32 v71, v90, v91
	v_cvt_pk_bf16_f32 v72, v72, v73
	v_cvt_pk_bf16_f32 v73, v74, v75
	v_cvt_pk_bf16_f32 v74, v78, v79
	v_cvt_pk_bf16_f32 v75, v80, v81
	v_cvt_pk_bf16_f32 v76, v82, v83
	v_cvt_pk_bf16_f32 v77, v84, v85
	global_store_dwordx4 v[86:87], v[70:73], off
	global_store_dwordx4 v[86:87], v[74:77], off offset:32

.LBB0_457:
	s_movk_i32 s2, 0x3fff
	v_cmp_lt_i32_e32 vcc, s2, v28
	s_mov_b64 s[20:21], 0
	s_and_saveexec_b64 s[2:3], vcc
	s_xor_b64 s[16:17], exec, s[2:3]
	s_cbranch_execz .LBB0_459
	v_add_u32_e32 v2, 0xffffc000, v28
	v_lshlrev_b64 v[4:5], 12, v[2:3]
	v_lshl_add_u64 v[16:17], v[24:25], 0, v[4:5]
	v_add_u32_e32 v55, s6, v28
	v_cmp_gt_i32_e32 vcc, 0x8000, v55
	v_lshl_add_u64 v[52:53], v[16:17], 0, s[10:11]
	s_nop 0
	v_cndmask_b32_e32 v52, v16, v52, vcc
	v_cndmask_b32_e32 v53, v17, v53, vcc
	global_load_dwordx4 v[4:7], v[16:17], off nt
	global_load_dwordx4 v[8:11], v[16:17], off offset:16 nt
	global_load_dwordx4 v[12:15], v[16:17], off offset:32 nt
	s_nop 0
	global_load_dwordx4 v[16:19], v[16:17], off offset:48 nt
	global_load_dword v54, v[52:53], off
	v_mbcnt_hi_u32_b32 v1, -1, v197
	v_and_b32_e32 v20, 64, v1
	v_xor_b32_e32 v21, 1, v1
	v_add_u32_e32 v20, 64, v20
	v_cmp_lt_i32_e32 vcc, v21, v20
	v_xor_b32_e32 v23, 2, v1
	s_and_b64 s[20:21], s[4:5], exec
	v_cndmask_b32_e32 v21, v1, v21, vcc
	v_lshlrev_b32_e32 v21, 2, v21
	v_cmp_lt_i32_e32 vcc, v23, v20
	s_waitcnt vmcnt(4)
	v_max3_f32 v22, |v4|, 0, |v5|
	v_max3_f32 v22, v22, |v6|, |v7|
	s_waitcnt vmcnt(3)
	v_max3_f32 v22, v22, |v8|, |v9|
	v_max3_f32 v22, v22, |v10|, |v11|
	s_waitcnt vmcnt(2)
	v_max3_f32 v22, v22, |v12|, |v13|
	v_max3_f32 v22, v22, |v14|, |v15|
	s_waitcnt vmcnt(1)
	v_max3_f32 v22, v22, |v16|, |v17|
	v_max3_f32 v22, v22, |v18|, |v19|
	ds_bpermute_b32 v21, v21, v22
	v_cndmask_b32_e32 v23, v1, v23, vcc
	v_lshlrev_b32_e32 v23, 2, v23
	s_waitcnt lgkmcnt(0)
	v_max_f32_e32 v21, v21, v21
	v_max_f32_e32 v21, v22, v21
	ds_bpermute_b32 v22, v23, v21
	v_xor_b32_e32 v23, 4, v1
	v_cmp_lt_i32_e32 vcc, v23, v20
	s_waitcnt lgkmcnt(0)
	v_max_f32_e32 v22, v22, v22
	v_cndmask_b32_e32 v23, v1, v23, vcc
	v_lshlrev_b32_e32 v23, 2, v23
	v_max_f32_e32 v21, v21, v22
	ds_bpermute_b32 v22, v23, v21
	v_xor_b32_e32 v23, 8, v1
	v_cmp_lt_i32_e32 vcc, v23, v20
	s_waitcnt lgkmcnt(0)
	v_max_f32_e32 v22, v22, v22
	v_cndmask_b32_e32 v23, v1, v23, vcc
	v_lshlrev_b32_e32 v23, 2, v23
	v_max_f32_e32 v21, v21, v22
	ds_bpermute_b32 v22, v23, v21
	v_xor_b32_e32 v23, 16, v1
	v_cmp_lt_i32_e32 vcc, v23, v20
	s_waitcnt lgkmcnt(0)
	v_max_f32_e32 v22, v22, v22
	v_cndmask_b32_e32 v23, v1, v23, vcc
	v_lshlrev_b32_e32 v23, 2, v23
	v_max_f32_e32 v21, v21, v22
	ds_bpermute_b32 v22, v23, v21
	v_xor_b32_e32 v23, 32, v1
	v_cmp_lt_i32_e32 vcc, v23, v20
	s_waitcnt lgkmcnt(0)
	v_max_f32_e32 v20, v22, v22
	v_cndmask_b32_e32 v1, v1, v23, vcc
	v_lshlrev_b32_e32 v1, 2, v1
	v_max_f32_e32 v23, v21, v20
	ds_bpermute_b32 v1, v1, v23
	v_mov_b32_e32 v20, v3
	v_mov_b32_e32 v21, v3
	v_mov_b32_e32 v22, v3
	s_waitcnt lgkmcnt(0)
	v_max_f32_e32 v1, v1, v1
	v_max_f32_e32 v1, v23, v1
	v_div_scale_f32 v34, s[2:3], v1, v1, s86
	v_rcp_f32_e32 v35, v34
	v_div_scale_f32 v36, vcc, s86, v1, s86
	v_cmp_lt_f32_e64 s[14:15], 0, v1
	v_fma_f32 v37, -v34, v35, 1.0
	v_fmac_f32_e32 v35, v37, v35
	v_mul_f32_e32 v37, v36, v35
	v_fma_f32 v38, -v34, v37, v36
	v_fmac_f32_e32 v37, v38, v35
	v_fma_f32 v34, -v34, v37, v36
	v_div_fmas_f32 v34, v34, v35, v37
	v_div_fixup_f32 v34, v34, v1, s86
	v_cndmask_b32_e64 v34, 1.0, v34, s[14:15]
	v_mov_b32_e32 v23, v3
	v_mul_f32_e32 v4, v4, v34
	v_mul_f32_e32 v5, v5, v34
	v_mul_f32_e32 v8, v8, v34
	v_mul_f32_e32 v9, v9, v34
	v_mul_f32_e32 v12, v12, v34
	v_mul_f32_e32 v13, v13, v34
	v_mul_f32_e32 v16, v16, v34
	v_mul_f32_e32 v17, v17, v34
	v_cvt_pk_fp8_f32 v20, v4, v5
	v_cvt_pk_fp8_f32 v21, v8, v9
	v_cvt_pk_fp8_f32 v22, v12, v13
	v_cvt_pk_fp8_f32 v23, v16, v17
	v_mul_f32_e32 v6, v6, v34
	v_mul_f32_e32 v7, v7, v34
	v_mul_f32_e32 v10, v10, v34
	v_mul_f32_e32 v11, v11, v34
	v_mul_f32_e32 v14, v14, v34
	v_mul_f32_e32 v15, v15, v34
	v_mul_f32_e32 v18, v18, v34
	v_mul_f32_e32 v19, v19, v34
	v_cvt_pk_fp8_f32 v20, v6, v7 op_sel:[0,0,1]
	v_cvt_pk_fp8_f32 v21, v10, v11 op_sel:[0,0,1]
	v_cvt_pk_fp8_f32 v22, v14, v15 op_sel:[0,0,1]
	v_cvt_pk_fp8_f32 v23, v18, v19 op_sel:[0,0,1]
	v_lshlrev_b64 v[4:5], 10, v[2:3]
	v_lshl_add_u64 v[4:5], v[26:27], 0, v[4:5]
	global_store_dwordx4 v[4:5], v[20:23], off
	v_mov_b64_e32 v[4:5], v[2:3]
.LBB0_459:
	s_or_saveexec_b64 s[16:17], s[16:17]
	v_readlane_b32 s24, v253, 0
	v_readlane_b32 s28, v253, 4
	v_readlane_b32 s29, v253, 5
	v_readlane_b32 s25, v253, 1
	v_readlane_b32 s26, v253, 2
	v_mov_b64_e32 v[34:35], s[28:29]
	v_readlane_b32 s27, v253, 3
	v_readlane_b32 s30, v253, 6
	v_readlane_b32 s31, v253, 7
	s_xor_b64 exec, exec, s[16:17]
	s_cbranch_execz .LBB0_461
	v_add_u32_e32 v55, s6, v28
	v_cmp_gt_i32_e32 vcc, 0x4000, v55
	v_lshl_add_u64 v[52:53], v[32:33], 0, s[10:11]
	s_nop 0
	v_cndmask_b32_e32 v52, v32, v52, vcc
	v_cndmask_b32_e32 v53, v33, v53, vcc
	global_load_dwordx4 v[16:19], v[32:33], off offset:-32 nt
	global_load_dwordx4 v[12:15], v[32:33], off offset:-16 nt
	global_load_dwordx4 v[8:11], v[32:33], off nt
	global_load_dwordx4 v[4:7], v[32:33], off offset:16 nt
	global_load_dword v54, v[52:53], off
	v_mbcnt_hi_u32_b32 v1, -1, v197
	v_and_b32_e32 v2, 64, v1
	v_xor_b32_e32 v23, 1, v1
	v_add_u32_e32 v2, 64, v2
	v_cmp_lt_i32_e32 vcc, v23, v2
	v_xor_b32_e32 v35, 2, v1
	s_andn2_b64 s[2:3], s[14:15], exec
	v_cndmask_b32_e32 v23, v1, v23, vcc
	v_lshlrev_b32_e32 v23, 2, v23
	v_cmp_lt_i32_e32 vcc, v35, v2
	s_andn2_b64 s[14:15], s[20:21], exec
	v_mov_b32_e32 v20, v3
	v_cndmask_b32_e32 v35, v1, v35, vcc
	v_lshlrev_b32_e32 v35, 2, v35
	v_mov_b32_e32 v21, v3
	v_mov_b32_e32 v22, v3
	v_readlane_b32 s24, v253, 0
	v_readlane_b32 s26, v253, 2
	v_readlane_b32 s27, v253, 3
	v_readlane_b32 s25, v253, 1
	v_readlane_b32 s28, v253, 4
	v_readlane_b32 s29, v253, 5
	v_readlane_b32 s30, v253, 6
	v_readlane_b32 s31, v253, 7
	s_waitcnt vmcnt(4)
	v_max3_f32 v34, |v16|, 0, |v17|
	v_max3_f32 v34, v34, |v18|, |v19|
	s_waitcnt vmcnt(3)
	v_max3_f32 v34, v34, |v12|, |v13|
	v_max3_f32 v34, v34, |v14|, |v15|
	s_waitcnt vmcnt(2)
	v_max3_f32 v34, v34, |v8|, |v9|
	v_max3_f32 v34, v34, |v10|, |v11|
	s_waitcnt vmcnt(1)
	v_max3_f32 v34, v34, |v4|, |v5|
	v_max3_f32 v34, v34, |v6|, |v7|
	ds_bpermute_b32 v23, v23, v34
	s_waitcnt lgkmcnt(0)
	v_max_f32_e32 v23, v23, v23
	v_max_f32_e32 v23, v34, v23
	ds_bpermute_b32 v34, v35, v23
	v_xor_b32_e32 v35, 4, v1
	v_cmp_lt_i32_e32 vcc, v35, v2
	s_waitcnt lgkmcnt(0)
	v_max_f32_e32 v34, v34, v34
	v_cndmask_b32_e32 v35, v1, v35, vcc
	v_lshlrev_b32_e32 v35, 2, v35
	v_max_f32_e32 v23, v23, v34
	ds_bpermute_b32 v34, v35, v23
	v_xor_b32_e32 v35, 8, v1
	v_cmp_lt_i32_e32 vcc, v35, v2
	s_waitcnt lgkmcnt(0)
	v_max_f32_e32 v34, v34, v34
	v_cndmask_b32_e32 v35, v1, v35, vcc
	v_lshlrev_b32_e32 v35, 2, v35
	v_max_f32_e32 v23, v23, v34
	ds_bpermute_b32 v34, v35, v23
	v_xor_b32_e32 v35, 16, v1
	v_cmp_lt_i32_e32 vcc, v35, v2
	s_waitcnt lgkmcnt(0)
	v_max_f32_e32 v34, v34, v34
	v_cndmask_b32_e32 v35, v1, v35, vcc
	v_lshlrev_b32_e32 v35, 2, v35
	v_max_f32_e32 v23, v23, v34
	ds_bpermute_b32 v34, v35, v23
	v_xor_b32_e32 v35, 32, v1
	v_cmp_lt_i32_e32 vcc, v35, v2
	s_waitcnt lgkmcnt(0)
	v_max_f32_e32 v2, v34, v34
	v_cndmask_b32_e32 v1, v1, v35, vcc
	v_lshlrev_b32_e32 v1, 2, v1
	v_max_f32_e32 v2, v23, v2
	ds_bpermute_b32 v1, v1, v2
	v_mov_b32_e32 v23, v3
	v_mov_b64_e32 v[34:35], s[26:27]
	s_waitcnt lgkmcnt(0)
	v_max_f32_e32 v1, v1, v1
	v_max_f32_e32 v1, v2, v1
	v_div_scale_f32 v2, s[20:21], v1, v1, s86
	v_rcp_f32_e32 v36, v2
	v_div_scale_f32 v37, vcc, s86, v1, s86
	s_and_b64 s[20:21], s[4:5], exec
	v_fma_f32 v38, -v2, v36, 1.0
	v_fmac_f32_e32 v36, v38, v36
	v_mul_f32_e32 v38, v37, v36
	v_fma_f32 v39, -v2, v38, v37
	v_fmac_f32_e32 v38, v39, v36
	v_fma_f32 v2, -v2, v38, v37
	v_div_fmas_f32 v2, v2, v36, v38
	v_div_fixup_f32 v2, v2, v1, s86
	v_cmp_lt_f32_e32 vcc, 0, v1
	s_or_b64 s[20:21], s[14:15], s[20:21]
	s_and_b64 s[14:15], vcc, exec
	v_cndmask_b32_e32 v2, 1.0, v2, vcc
	v_mul_f32_e32 v16, v16, v2
	v_mul_f32_e32 v17, v17, v2
	v_mul_f32_e32 v12, v12, v2
	v_mul_f32_e32 v13, v13, v2
	v_mul_f32_e32 v8, v8, v2
	v_mul_f32_e32 v9, v9, v2
	v_mul_f32_e32 v4, v4, v2
	v_mul_f32_e32 v5, v5, v2
	v_cvt_pk_fp8_f32 v20, v16, v17
	v_cvt_pk_fp8_f32 v21, v12, v13
	v_cvt_pk_fp8_f32 v22, v8, v9
	v_cvt_pk_fp8_f32 v23, v4, v5
	v_mul_f32_e32 v18, v18, v2
	v_mul_f32_e32 v19, v19, v2
	v_mul_f32_e32 v14, v14, v2
	v_mul_f32_e32 v15, v15, v2
	v_mul_f32_e32 v10, v10, v2
	v_mul_f32_e32 v11, v11, v2
	v_mul_f32_e32 v6, v6, v2
	v_mul_f32_e32 v2, v7, v2
	v_cvt_pk_fp8_f32 v20, v18, v19 op_sel:[0,0,1]
	v_cvt_pk_fp8_f32 v21, v14, v15 op_sel:[0,0,1]
	v_cvt_pk_fp8_f32 v22, v10, v11 op_sel:[0,0,1]
	v_cvt_pk_fp8_f32 v23, v6, v2 op_sel:[0,0,1]
	s_or_b64 s[14:15], s[2:3], s[14:15]
	v_mov_b64_e32 v[4:5], v[28:29]
	global_store_dwordx4 v[30:31], v[20:23], off
